# v39 + PEER gather queues: a wave whose own XCD queue is exhausted stops instead of taking tail items from other XCDs' queues (those ran against a cold L2)
# speedup vs baseline: 1.0113x; 1.0113x over previous
.LBB0_1986:
	s_mov_b64 s[6:7], -1
	s_cmp_gt_i32 s17, -1
	s_mov_b64 s[12:13], -1
	s_cbranch_scc1 .LBB0_1985
	v_mov_b32_e32 v20, 0
	s_and_saveexec_b64 s[6:7], s[4:5]
	s_cbranch_execz .LBB0_1984
	s_and_b32 s12, s14, 0x1c0
	s_lshl_b32 s12, s12, 2
	v_mov_b32_e32 v20, s12
	global_atomic_add v20, v20, v227, s[2:3] sc0
	s_branch .LBB0_1984

.LBB0_2167:
	s_mov_b64 s[6:7], -1
	s_cmp_gt_i32 s15, -1
	s_mov_b64 s[8:9], -1
	s_cbranch_scc1 .LBB0_2166
	v_mov_b32_e32 v20, 0
	s_and_saveexec_b64 s[6:7], s[4:5]
	s_cbranch_execz .LBB0_2165
	s_and_b32 s8, s10, 0x1c0
	s_lshl_b32 s8, s8, 2
	v_mov_b32_e32 v20, s8
	global_atomic_add v20, v20, v227, s[2:3] sc0
	s_branch .LBB0_2165
